# F fp8 epilogue rewritten by hand: store-friendly OB column permutation (F writes, G reads), in-wave ds_bpermute lane transpose so 4 adjacent lanes store 64 contiguous bytes, 32-bit saddr addressing
# speedup vs baseline: 1.0001x; 1.0001x over previous
.LBB0_2677:
	v_mov_b32_e32 v2, v0
	s_cmp_eq_u32 s24, 64
	v_bfe_u32 v148, v2, 4, 2
	v_and_or_b32 v147, v2, 15, s58
	s_mov_b64 s[24:25], -1
	s_cbranch_scc1 .LBB0_2696
	v_and_b32_e32 v150, 63, v2
	v_lshrrev_b32_e32 v151, 2, v150
	v_and_b32_e32 v152, 3, v150
	v_or_b32_e32 v147, s58, v151
	v_lshlrev_b32_e32 v149, 11, v147
	v_lshl_or_b32 v149, v152, 4, v149
	v_and_b32_e32 v153, 0x3c, v150
	v_lshl_or_b32 v153, v152, 6, v153
	s_ashr_i32 s19, s18, 31
	s_add_u32 s18, s6, s18
	s_addc_u32 s19, s7, s19
	s_lshl_b32 s98, s8, 1
	s_add_u32 s18, s18, s98
	s_addc_u32 s19, s19, 0
	s_lshl_b32 s98, s10, 11
	s_add_u32 s18, s18, s98
	s_addc_u32 s19, s19, 0
	v_pk_mul_f32 v[160:161], v[128:129], s[74:75] op_sel_hi:[1,0]
	v_pk_mul_f32 v[162:163], v[130:131], s[74:75] op_sel_hi:[1,0]
	v_pk_mul_f32 v[164:165], v[124:125], s[74:75] op_sel_hi:[1,0]
	v_pk_mul_f32 v[166:167], v[126:127], s[74:75] op_sel_hi:[1,0]
	v_pk_mul_f32 v[168:169], v[120:121], s[74:75] op_sel_hi:[1,0]
	v_pk_mul_f32 v[170:171], v[122:123], s[74:75] op_sel_hi:[1,0]
	v_pk_mul_f32 v[172:173], v[112:113], s[74:75] op_sel_hi:[1,0]
	v_pk_mul_f32 v[174:175], v[114:115], s[74:75] op_sel_hi:[1,0]
	v_cvt_pk_fp8_f32 v132, v160, v161
	v_cvt_pk_fp8_f32 v133, v164, v165
	v_cvt_pk_fp8_f32 v134, v168, v169
	v_cvt_pk_fp8_f32 v135, v172, v173
	v_cvt_pk_fp8_f32 v132, v162, v163 op_sel:[0,0,1]
	v_cvt_pk_fp8_f32 v133, v166, v167 op_sel:[0,0,1]
	v_cvt_pk_fp8_f32 v134, v170, v171 op_sel:[0,0,1]
	v_cvt_pk_fp8_f32 v135, v174, v175 op_sel:[0,0,1]
	s_nop 0
	ds_bpermute_b32 v180, v153, v132
	ds_bpermute_b32 v181, v153, v133
	ds_bpermute_b32 v182, v153, v134
	ds_bpermute_b32 v183, v153, v135
	v_pk_mul_f32 v[160:161], v[116:117], s[74:75] op_sel_hi:[1,0]
	v_pk_mul_f32 v[162:163], v[118:119], s[74:75] op_sel_hi:[1,0]
	v_pk_mul_f32 v[164:165], v[108:109], s[74:75] op_sel_hi:[1,0]
	v_pk_mul_f32 v[166:167], v[110:111], s[74:75] op_sel_hi:[1,0]
	v_pk_mul_f32 v[168:169], v[104:105], s[74:75] op_sel_hi:[1,0]
	v_pk_mul_f32 v[170:171], v[106:107], s[74:75] op_sel_hi:[1,0]
	v_pk_mul_f32 v[172:173], v[96:97], s[74:75] op_sel_hi:[1,0]
	v_pk_mul_f32 v[174:175], v[98:99], s[74:75] op_sel_hi:[1,0]
	v_cvt_pk_fp8_f32 v176, v160, v161
	v_cvt_pk_fp8_f32 v177, v164, v165
	v_cvt_pk_fp8_f32 v178, v168, v169
	v_cvt_pk_fp8_f32 v179, v172, v173
	v_cvt_pk_fp8_f32 v176, v162, v163 op_sel:[0,0,1]
	v_cvt_pk_fp8_f32 v177, v166, v167 op_sel:[0,0,1]
	v_cvt_pk_fp8_f32 v178, v170, v171 op_sel:[0,0,1]
	v_cvt_pk_fp8_f32 v179, v174, v175 op_sel:[0,0,1]
	s_nop 0
	ds_bpermute_b32 v184, v153, v176
	ds_bpermute_b32 v185, v153, v177
	ds_bpermute_b32 v186, v153, v178
	ds_bpermute_b32 v187, v153, v179
	s_waitcnt lgkmcnt(4)
	v_cmp_gt_i32_e32 vcc, s11, v147
	s_nop 0
	s_and_saveexec_b64 s[24:25], vcc
	global_store_dwordx4 v149, v[180:183], s[18:19]
	s_or_b64 exec, exec, s[24:25]
	v_add_u32_e32 v149, 0x8000, v149
	v_pk_mul_f32 v[160:161], v[100:101], s[74:75] op_sel_hi:[1,0]
	v_pk_mul_f32 v[162:163], v[102:103], s[74:75] op_sel_hi:[1,0]
	v_pk_mul_f32 v[164:165], v[92:93], s[74:75] op_sel_hi:[1,0]
	v_pk_mul_f32 v[166:167], v[94:95], s[74:75] op_sel_hi:[1,0]
	v_pk_mul_f32 v[168:169], v[88:89], s[74:75] op_sel_hi:[1,0]
	v_pk_mul_f32 v[170:171], v[90:91], s[74:75] op_sel_hi:[1,0]
	v_pk_mul_f32 v[172:173], v[80:81], s[74:75] op_sel_hi:[1,0]
	v_pk_mul_f32 v[174:175], v[82:83], s[74:75] op_sel_hi:[1,0]
	v_cvt_pk_fp8_f32 v132, v160, v161
	v_cvt_pk_fp8_f32 v133, v164, v165
	v_cvt_pk_fp8_f32 v134, v168, v169
	v_cvt_pk_fp8_f32 v135, v172, v173
	v_cvt_pk_fp8_f32 v132, v162, v163 op_sel:[0,0,1]
	v_cvt_pk_fp8_f32 v133, v166, v167 op_sel:[0,0,1]
	v_cvt_pk_fp8_f32 v134, v170, v171 op_sel:[0,0,1]
	v_cvt_pk_fp8_f32 v135, v174, v175 op_sel:[0,0,1]
	s_nop 0
	ds_bpermute_b32 v180, v153, v132
	ds_bpermute_b32 v181, v153, v133
	ds_bpermute_b32 v182, v153, v134
	ds_bpermute_b32 v183, v153, v135
	s_waitcnt lgkmcnt(4)
	s_sub_i32 s98, s11, 16
	v_cmp_gt_i32_e32 vcc, s98, v147
	s_nop 0
	s_and_saveexec_b64 s[24:25], vcc
	global_store_dwordx4 v149, v[184:187], s[18:19]
	s_or_b64 exec, exec, s[24:25]
	v_add_u32_e32 v149, 0x8000, v149
	v_pk_mul_f32 v[160:161], v[84:85], s[74:75] op_sel_hi:[1,0]
	v_pk_mul_f32 v[162:163], v[86:87], s[74:75] op_sel_hi:[1,0]
	v_pk_mul_f32 v[164:165], v[76:77], s[74:75] op_sel_hi:[1,0]
	v_pk_mul_f32 v[166:167], v[78:79], s[74:75] op_sel_hi:[1,0]
	v_pk_mul_f32 v[168:169], v[72:73], s[74:75] op_sel_hi:[1,0]
	v_pk_mul_f32 v[170:171], v[74:75], s[74:75] op_sel_hi:[1,0]
	v_pk_mul_f32 v[172:173], v[68:69], s[74:75] op_sel_hi:[1,0]
	v_pk_mul_f32 v[174:175], v[70:71], s[74:75] op_sel_hi:[1,0]
	v_cvt_pk_fp8_f32 v176, v160, v161
	v_cvt_pk_fp8_f32 v177, v164, v165
	v_cvt_pk_fp8_f32 v178, v168, v169
	v_cvt_pk_fp8_f32 v179, v172, v173
	v_cvt_pk_fp8_f32 v176, v162, v163 op_sel:[0,0,1]
	v_cvt_pk_fp8_f32 v177, v166, v167 op_sel:[0,0,1]
	v_cvt_pk_fp8_f32 v178, v170, v171 op_sel:[0,0,1]
	v_cvt_pk_fp8_f32 v179, v174, v175 op_sel:[0,0,1]
	s_nop 0
	ds_bpermute_b32 v184, v153, v176
	ds_bpermute_b32 v185, v153, v177
	ds_bpermute_b32 v186, v153, v178
	ds_bpermute_b32 v187, v153, v179
	s_waitcnt lgkmcnt(4)
	s_sub_i32 s98, s11, 32
	v_cmp_gt_i32_e32 vcc, s98, v147
	s_nop 0
	s_and_saveexec_b64 s[24:25], vcc
	global_store_dwordx4 v149, v[180:183], s[18:19]
	s_or_b64 exec, exec, s[24:25]
	v_add_u32_e32 v149, 0x8000, v149
	v_pk_mul_f32 v[160:161], v[64:65], s[74:75] op_sel_hi:[1,0]
	v_pk_mul_f32 v[162:163], v[66:67], s[74:75] op_sel_hi:[1,0]
	v_pk_mul_f32 v[164:165], v[60:61], s[74:75] op_sel_hi:[1,0]
	v_pk_mul_f32 v[166:167], v[62:63], s[74:75] op_sel_hi:[1,0]
	v_pk_mul_f32 v[168:169], v[56:57], s[74:75] op_sel_hi:[1,0]
	v_pk_mul_f32 v[170:171], v[58:59], s[74:75] op_sel_hi:[1,0]
	v_pk_mul_f32 v[172:173], v[48:49], s[74:75] op_sel_hi:[1,0]
	v_pk_mul_f32 v[174:175], v[50:51], s[74:75] op_sel_hi:[1,0]
	v_cvt_pk_fp8_f32 v132, v160, v161
	v_cvt_pk_fp8_f32 v133, v164, v165
	v_cvt_pk_fp8_f32 v134, v168, v169
	v_cvt_pk_fp8_f32 v135, v172, v173
	v_cvt_pk_fp8_f32 v132, v162, v163 op_sel:[0,0,1]
	v_cvt_pk_fp8_f32 v133, v166, v167 op_sel:[0,0,1]
	v_cvt_pk_fp8_f32 v134, v170, v171 op_sel:[0,0,1]
	v_cvt_pk_fp8_f32 v135, v174, v175 op_sel:[0,0,1]
	s_nop 0
	ds_bpermute_b32 v180, v153, v132
	ds_bpermute_b32 v181, v153, v133
	ds_bpermute_b32 v182, v153, v134
	ds_bpermute_b32 v183, v153, v135
	s_waitcnt lgkmcnt(4)
	s_sub_i32 s98, s11, 48
	v_cmp_gt_i32_e32 vcc, s98, v147
	s_nop 0
	s_and_saveexec_b64 s[24:25], vcc
	global_store_dwordx4 v149, v[184:187], s[18:19]
	s_or_b64 exec, exec, s[24:25]
	v_add_u32_e32 v149, 0x28000, v149
	v_pk_mul_f32 v[160:161], v[52:53], s[74:75] op_sel_hi:[1,0]
	v_pk_mul_f32 v[162:163], v[54:55], s[74:75] op_sel_hi:[1,0]
	v_pk_mul_f32 v[164:165], v[44:45], s[74:75] op_sel_hi:[1,0]
	v_pk_mul_f32 v[166:167], v[46:47], s[74:75] op_sel_hi:[1,0]
	v_pk_mul_f32 v[168:169], v[40:41], s[74:75] op_sel_hi:[1,0]
	v_pk_mul_f32 v[170:171], v[42:43], s[74:75] op_sel_hi:[1,0]
	v_pk_mul_f32 v[172:173], v[32:33], s[74:75] op_sel_hi:[1,0]
	v_pk_mul_f32 v[174:175], v[34:35], s[74:75] op_sel_hi:[1,0]
	v_cvt_pk_fp8_f32 v176, v160, v161
	v_cvt_pk_fp8_f32 v177, v164, v165
	v_cvt_pk_fp8_f32 v178, v168, v169
	v_cvt_pk_fp8_f32 v179, v172, v173
	v_cvt_pk_fp8_f32 v176, v162, v163 op_sel:[0,0,1]
	v_cvt_pk_fp8_f32 v177, v166, v167 op_sel:[0,0,1]
	v_cvt_pk_fp8_f32 v178, v170, v171 op_sel:[0,0,1]
	v_cvt_pk_fp8_f32 v179, v174, v175 op_sel:[0,0,1]
	s_nop 0
	ds_bpermute_b32 v184, v153, v176
	ds_bpermute_b32 v185, v153, v177
	ds_bpermute_b32 v186, v153, v178
	ds_bpermute_b32 v187, v153, v179
	s_waitcnt lgkmcnt(4)
	s_sub_i32 s98, s11, 128
	v_cmp_gt_i32_e32 vcc, s98, v147
	s_nop 0
	s_and_saveexec_b64 s[24:25], vcc
	global_store_dwordx4 v149, v[180:183], s[18:19]
	s_or_b64 exec, exec, s[24:25]
	v_add_u32_e32 v149, 0x8000, v149
	v_pk_mul_f32 v[160:161], v[36:37], s[74:75] op_sel_hi:[1,0]
	v_pk_mul_f32 v[162:163], v[38:39], s[74:75] op_sel_hi:[1,0]
	v_pk_mul_f32 v[164:165], v[28:29], s[74:75] op_sel_hi:[1,0]
	v_pk_mul_f32 v[166:167], v[30:31], s[74:75] op_sel_hi:[1,0]
	v_pk_mul_f32 v[168:169], v[24:25], s[74:75] op_sel_hi:[1,0]
	v_pk_mul_f32 v[170:171], v[26:27], s[74:75] op_sel_hi:[1,0]
	v_pk_mul_f32 v[172:173], v[16:17], s[74:75] op_sel_hi:[1,0]
	v_pk_mul_f32 v[174:175], v[18:19], s[74:75] op_sel_hi:[1,0]
	v_cvt_pk_fp8_f32 v132, v160, v161
	v_cvt_pk_fp8_f32 v133, v164, v165
	v_cvt_pk_fp8_f32 v134, v168, v169
	v_cvt_pk_fp8_f32 v135, v172, v173
	v_cvt_pk_fp8_f32 v132, v162, v163 op_sel:[0,0,1]
	v_cvt_pk_fp8_f32 v133, v166, v167 op_sel:[0,0,1]
	v_cvt_pk_fp8_f32 v134, v170, v171 op_sel:[0,0,1]
	v_cvt_pk_fp8_f32 v135, v174, v175 op_sel:[0,0,1]
	s_nop 0
	ds_bpermute_b32 v180, v153, v132
	ds_bpermute_b32 v181, v153, v133
	ds_bpermute_b32 v182, v153, v134
	ds_bpermute_b32 v183, v153, v135
	s_waitcnt lgkmcnt(4)
	s_sub_i32 s98, s11, 144
	v_cmp_gt_i32_e32 vcc, s98, v147
	s_nop 0
	s_and_saveexec_b64 s[24:25], vcc
	global_store_dwordx4 v149, v[184:187], s[18:19]
	s_or_b64 exec, exec, s[24:25]
	v_add_u32_e32 v149, 0x8000, v149
	v_pk_mul_f32 v[160:161], v[20:21], s[74:75] op_sel_hi:[1,0]
	v_pk_mul_f32 v[162:163], v[22:23], s[74:75] op_sel_hi:[1,0]
	v_pk_mul_f32 v[164:165], v[12:13], s[74:75] op_sel_hi:[1,0]
	v_pk_mul_f32 v[166:167], v[14:15], s[74:75] op_sel_hi:[1,0]
	v_pk_mul_f32 v[168:169], v[8:9], s[74:75] op_sel_hi:[1,0]
	v_pk_mul_f32 v[170:171], v[10:11], s[74:75] op_sel_hi:[1,0]
	v_pk_mul_f32 v[172:173], v[4:5], s[74:75] op_sel_hi:[1,0]
	v_pk_mul_f32 v[174:175], v[6:7], s[74:75] op_sel_hi:[1,0]
	v_cvt_pk_fp8_f32 v176, v160, v161
	v_cvt_pk_fp8_f32 v177, v164, v165
	v_cvt_pk_fp8_f32 v178, v168, v169
	v_cvt_pk_fp8_f32 v179, v172, v173
	v_cvt_pk_fp8_f32 v176, v162, v163 op_sel:[0,0,1]
	v_cvt_pk_fp8_f32 v177, v166, v167 op_sel:[0,0,1]
	v_cvt_pk_fp8_f32 v178, v170, v171 op_sel:[0,0,1]
	v_cvt_pk_fp8_f32 v179, v174, v175 op_sel:[0,0,1]
	s_nop 0
	ds_bpermute_b32 v184, v153, v176
	ds_bpermute_b32 v185, v153, v177
	ds_bpermute_b32 v186, v153, v178
	ds_bpermute_b32 v187, v153, v179
	s_waitcnt lgkmcnt(4)
	s_sub_i32 s98, s11, 160
	v_cmp_gt_i32_e32 vcc, s98, v147
	s_nop 0
	s_and_saveexec_b64 s[24:25], vcc
	global_store_dwordx4 v149, v[180:183], s[18:19]
	s_or_b64 exec, exec, s[24:25]
	v_add_u32_e32 v149, 0x8000, v149
	s_waitcnt lgkmcnt(0)
	s_sub_i32 s98, s11, 176
	v_cmp_gt_i32_e32 vcc, s98, v147
	s_nop 0
	s_and_saveexec_b64 s[24:25], vcc
	global_store_dwordx4 v149, v[184:187], s[18:19]
	s_or_b64 exec, exec, s[24:25]

.LBB0_2903:
	s_or_b64 exec, exec, s[14:15]
	s_andn2_b64 vcc, exec, s[12:13]
	s_cbranch_vccnz .LBB0_2918
	s_cmp_eq_u32 s36, 3
	s_mov_b64 s[14:15], s[70:71]
	s_cselect_b32 s17, s15, 0
	s_cselect_b32 s16, s14, 0
	s_lshl_b32 s12, s37, 13
	v_and_b32_e32 v2, 32, v102
	v_and_b32_e32 v4, 15, v102
	v_lshlrev_b32_e32 v2, 3, v2
	v_lshl_or_b32 v2, v4, 4, v2
	v_and_b32_e32 v4, 16, v102
	v_lshrrev_b32_e32 v4, 1, v4
	v_or_b32_e32 v2, v2, v4
	s_add_i32 s14, s12, 0
	v_lshl_add_u64 v[4:5], s[6:7], 0, v[2:3]
	s_mov_b64 s[12:13], 0x4fb00000
	v_and_b32_e32 v2, 64, v219
	v_lshl_add_u64 v[14:15], v[4:5], 0, s[12:13]
	v_add_u32_e32 v2, 64, v2
	v_xor_b32_e32 v4, 1, v219
	v_cmp_lt_i32_e32 vcc, v4, v2
	s_lshl_b32 s18, s36, 11
	s_ashr_i32 s19, s18, 31
	v_cndmask_b32_e32 v4, v219, v4, vcc
	v_lshlrev_b32_e32 v104, 2, v4
	v_xor_b32_e32 v4, 2, v219
	v_cmp_lt_i32_e32 vcc, v4, v2
	s_cmp_lg_u64 s[16:17], 0
	s_mov_b64 s[20:21], 0x4ae00000
	v_cndmask_b32_e32 v4, v219, v4, vcc
	v_lshlrev_b32_e32 v105, 2, v4
	v_xor_b32_e32 v4, 4, v219
	v_cmp_lt_i32_e32 vcc, v4, v2
	v_lshl_add_u32 v103, v102, 5, s14
	s_cselect_b64 s[12:13], -1, 0
	v_cndmask_b32_e32 v4, v219, v4, vcc
	v_lshlrev_b32_e32 v106, 2, v4
	v_xor_b32_e32 v4, 8, v219
	v_cmp_lt_i32_e32 vcc, v4, v2
	s_lshl_b32 s14, s5, 3
	s_ashr_i32 s5, s4, 31
	v_cndmask_b32_e32 v4, v219, v4, vcc
	v_lshlrev_b32_e32 v107, 2, v4
	v_xor_b32_e32 v4, 16, v219
	v_cmp_lt_i32_e32 vcc, v4, v2
	s_nop 1
	v_cndmask_b32_e32 v4, v219, v4, vcc
	v_lshlrev_b32_e32 v108, 2, v4
	v_xor_b32_e32 v4, 32, v219
	v_cmp_lt_i32_e32 vcc, v4, v2
	s_nop 1
	v_cndmask_b32_e32 v2, v219, v4, vcc
	v_lshlrev_b32_e32 v109, 2, v2
	v_lshlrev_b32_e32 v2, 4, v102
	v_lshl_add_u64 v[4:5], s[6:7], 0, v[2:3]
	v_lshl_add_u64 v[16:17], v[4:5], 0, s[20:21]
	s_mov_b64 s[20:21], 0x37e00000
	v_lshl_add_u64 v[18:19], v[4:5], 0, s[20:21]
	s_lshl_b64 s[20:21], s[4:5], 12
	s_add_u32 s6, s6, s20
	s_addc_u32 s7, s7, s21
	v_lshl_add_u64 v[4:5], s[6:7], 0, v[2:3]
	s_mov_b64 s[6:7], 0x3be00000
	v_lshlrev_b32_e32 v2, 5, v102
	s_lshl_b64 s[18:19], s[18:19], 2
	v_lshl_add_u64 v[20:21], v[4:5], 0, s[6:7]
	v_or_b32_e32 v4, s18, v2
	v_mov_b32_e32 v5, s19
	v_readlane_b32 s18, v242, 3
	s_ashr_i32 s15, s14, 31
	v_readlane_b32 s19, v242, 4
	s_lshl_b64 s[6:7], s[14:15], 12
	s_nop 0
	v_lshl_add_u64 v[22:23], s[18:19], 0, v[4:5]
	s_lshl_b64 s[18:19], s[4:5], 13
	s_add_u32 s16, s16, s18
	s_addc_u32 s17, s17, s19
	v_readlane_b32 s18, v242, 5
	v_readlane_b32 s19, v242, 6
	v_lshl_add_u64 v[24:25], s[16:17], 0, v[2:3]
	s_lshl_b64 s[16:17], s[14:15], 13
	v_lshl_add_u64 v[26:27], s[18:19], 0, v[4:5]
	s_branch .LBB0_2906
